# re-measure (same file as v54)
# speedup vs baseline: 1.0080x; 1.0080x over previous
.LBB0_789:
	s_or_b64 exec, exec, s[2:3]
	v_readlane_b32 s2, v253, 55
	s_waitcnt lgkmcnt(0)
	s_barrier
	v_mov_b32_e32 v0, s2
	v_readlane_b32 s2, v253, 54
	ds_read_b32 v0, v0
	s_nop 0
	v_mov_b32_e32 v1, s2
	ds_read_b32 v1, v1
	s_waitcnt lgkmcnt(0)
	s_barrier
	v_add_u32_e32 v201, 0x580, v0
	s_nop 0
	v_readfirstlane_b32 s100, v201
	v_readlane_b32 s101, v254, 38
	s_nop 3
	s_movk_i32 vcc_lo, 0x4c0
	s_movk_i32 vcc_hi, 0xc80
	s_cmp_eq_u32 s101, 0
	s_cselect_b32 vcc_lo, 0xac0, vcc_lo
	s_cselect_b32 vcc_hi, 0x1580, vcc_hi
	s_cmp_eq_u32 s101, 3
	s_cselect_b32 vcc_lo, 0, vcc_lo
	s_cselect_b32 vcc_hi, 0, vcc_hi
	s_add_i32 vcc_lo, s100, vcc_lo
	s_max_u32 vcc_lo, vcc_lo, vcc_hi
	v_mov_b32_e32 v201, vcc_lo
	v_readfirstlane_b32 s30, v0
	v_cmp_ge_i32_e32 vcc, v1, v201
	v_readfirstlane_b32 s24, v1
	s_cbranch_vccnz .LBB0_931
	s_add_u32 s31, s4, 0x37b00000
	s_addc_u32 s34, s5, 0
	s_add_i32 s35, s30, 0x480
	s_add_u32 s44, s4, 0x61800000
	s_addc_u32 s45, s5, 0
	s_add_u32 s46, s4, 0x42c00000
	s_addc_u32 s47, s5, 0
	s_add_u32 s10, s4, 0x66d00000
	s_addc_u32 s11, s5, 0
	s_add_u32 s48, s4, 0x61640000
	s_movk_i32 s2, 0x100
	s_addc_u32 s49, s5, 0
	v_cmp_gt_i32_e64 s[38:39], s2, v199
	s_add_i32 s2, 0, 0x14800
	v_add_u32_e32 v214, s2, v200
	s_add_i32 s2, 0, 0x16800
	s_cmp_lg_u32 0, -1
	v_lshlrev_b32_e32 v3, 1, v199
	v_lshlrev_b32_e32 v211, 4, v199
	s_cselect_b32 s3, 0, 0
	v_lshlrev_b32_e32 v0, 3, v199
	v_lshlrev_b32_e32 v1, 10, v101
	v_lshlrev_b32_e32 v2, 4, v198
	v_and_b32_e32 v3, 32, v3
	v_and_b32_e32 v5, 0xc0, v211
	s_addk_i32 s3, 0x6000
	v_and_b32_e32 v210, 24, v0
	v_lshl_or_b32 v5, v101, 8, v5
	v_add3_u32 v213, 0, v1, v2
	v_add_u32_e32 v1, s3, v3
	v_add3_u32 v217, v1, v210, v5
	v_lshrrev_b32_e32 v1, 3, v100
	v_lshl_add_u32 v215, v198, 2, s2
	v_and_b32_e32 v218, 56, v0
	v_lshl_add_u32 v220, v1, 2, s2
	s_add_i32 s2, 0, 0x14a00
	v_add_u32_e32 v4, 0, v3
	v_lshlrev_b32_e32 v96, 1, v218
	v_add_u32_e32 v221, s2, v200
	s_add_i32 s2, 0, 0x14900
	v_ashrrev_i32_e32 v203, 31, v202
	v_lshlrev_b32_e32 v208, 9, v100
	v_lshrrev_b32_e32 v209, 2, v100
	v_add3_u32 v212, v4, v210, v5
	v_cmp_gt_u32_e64 s[40:41], 32, v100
	v_cmp_lt_u32_e64 s[42:43], 31, v100
	v_or_b32_e32 v216, 0xc0, v206
	v_lshl_add_u64 v[204:205], s[4:5], 0, v[96:97]
	v_lshlrev_b32_e32 v219, 7, v1
	v_add_u32_e32 v222, s2, v200
	v_lshlrev_b32_e32 v96, 1, v98
	s_branch .LBB0_792

.LBB0_796:
	s_or_b64 exec, exec, s[2:3]
	v_readlane_b32 s101, v254, 38
	s_nop 3
	s_cmp_eq_u32 s101, 3
	s_cbranch_scc1 .Lc3_attn
	s_cmp_eq_u32 s101, 0
	s_cbranch_scc1 .Lc3_l0
	s_cmpk_lt_u32 s24, 0x600
	s_cbranch_scc0 .Lc3_rB
	s_lshr_b32 s101, s24, 2
	s_and_b32 s2, s24, 3
	s_cmp_eq_u32 s2, 3
	s_cbranch_scc1 .Lc3_entry
	s_sub_i32 s24, s24, s101
	s_branch .Lc3_chk
.Lc3_rB:
	s_cmpk_lt_u32 s24, 0xc80
	s_cbranch_scc0 .Lc3_late
	s_sub_i32 s2, s24, 0x600
	s_lshr_b32 s101, s2, 1
	s_bitcmp1_b32 s2, 0
	s_cbranch_scc0 .Lc3_rBa
	s_addk_i32 s101, 0x180
	s_branch .Lc3_entry
.Lc3_rBa:
	s_add_i32 s24, s101, 0x480
	s_branch .Lc3_chk
